# speedup vs baseline: 1.0096x; 1.0000x over previous
_ZN12_GLOBAL__N_113search_kernelEPKfS1_PhPf:
	s_load_dwordx2 s[8:9], s[0:1], 0x0
	s_load_dwordx2 s[4:5], s[0:1], 0x10
	s_movk_i32 s3, 0x90
	v_readfirstlane_b32 s10, v0
	v_cmp_gt_u32_e32 vcc, s3, v0
	s_and_saveexec_b64 s[6:7], vcc
	v_mov_b32_e32 v2, -1
	v_lshlrev_b32_e32 v1, 3, v0
	v_mov_b32_e32 v3, v2
	ds_write_b64 v1, v[2:3] offset:16384
	s_or_b64 exec, exec, s[6:7]
	s_waitcnt lgkmcnt(0)
	s_add_u32 s6, s4, 0x240000
	s_addc_u32 s7, s5, 0
	s_lshl_b32 s11, s2, 1
	s_and_b32 s14, s11, 14
	s_ashr_i32 s11, s2, 7
	s_lshr_b32 s15, s10, 6
	s_add_i32 s14, s14, s11
	s_bfe_u32 s2, s2, 0x40003
	s_mul_i32 s11, s15, 24
	v_mul_u32_u24_e32 v2, 0x71d, v0
	v_mul_u32_u24_e32 v4, 0x195, v0
	s_min_u32 s18, s11, 0xa5
	s_mul_i32 s11, s14, 3
	s_mul_i32 s12, s2, 9
	s_mov_b32 s13, 0
	v_lshrrev_b32_e32 v3, 16, v2
	s_movk_i32 s19, 0xffdc
	v_lshrrev_b32_e32 v5, 17, v4
	v_mad_i32_i24 v2, v3, s19, v0
	v_mad_i32_i24 v4, v5, -9, v3
	v_add_u32_e32 v3, s11, v5
	v_mov_b64_e32 v[6:7], s[12:13]
	v_mad_i64_i32 v[8:9], s[16:17], v3, s3, v[6:7]
	v_ashrrev_i32_e32 v5, 31, v4
	v_lshl_add_u64 v[4:5], v[8:9], 0, v[4:5]
	s_movk_i32 s13, 0x240
	v_mov_b64_e32 v[8:9], s[8:9]
	v_mad_u64_u32 v[10:11], s[8:9], v4, s13, v[8:9]
	v_min_u32_e32 v4, 0x1cb, v0
	v_or_b32_e32 v4, 0x200, v4
	v_mad_i32_i24 v11, v5, s13, v11
	v_mul_u32_u24_e32 v5, 0x71d, v4
	v_ashrrev_i32_e32 v3, 31, v2
	v_lshrrev_b32_e32 v5, 16, v5
	v_lshl_add_u64 v[2:3], v[2:3], 4, v[10:11]
	v_mad_i32_i24 v10, v5, s19, v4
	v_mul_u32_u24_e32 v4, 0x653, v4
	v_lshrrev_b32_e32 v11, 19, v4
	v_mad_i32_i24 v4, v11, -9, v5
	v_add_u32_e32 v5, s11, v11
	v_mad_i64_i32 v[6:7], s[8:9], v5, s3, v[6:7]
	v_ashrrev_i32_e32 v5, 31, v4
	v_lshl_add_u64 v[4:5], v[6:7], 0, v[4:5]
	v_mad_u64_u32 v[12:13], s[8:9], v4, s13, v[8:9]
	s_mul_i32 s8, s14, 0x90
	s_barrier
	global_load_dwordx4 v[6:9], v[2:3], off
	s_add_i32 s3, s8, s12
	v_and_b32_e32 v210, 15, v0
	v_lshlrev_b32_e32 v252, 3, v210
	v_bfe_u32 v253, v0, 4, 2
	s_lshl_b32 s11, s3, 6
	v_and_b32_e32 v2, 48, v0
	s_mul_i32 s9, s14, 0xbd
	v_or3_b32 v2, s11, v2, v210
	s_add_i32 s18, s18, s9
	v_and_b32_e32 v1, 63, v0
	v_ashrrev_i32_e32 v3, 31, v2
	s_lshl_b32 s3, s18, 6
	v_mad_i32_i24 v13, v5, s13, v13
	v_lshl_add_u64 v[14:15], v[2:3], 4, s[4:5]
	v_or_b32_e32 v2, s3, v1
	v_ashrrev_i32_e32 v11, 31, v10
	v_ashrrev_i32_e32 v3, 31, v2
	v_lshl_add_u64 v[10:11], v[10:11], 4, v[12:13]
	v_lshl_add_u64 v[16:17], v[2:3], 4, s[6:7]
	global_load_dwordx4 v[2:5], v[14:15], off
	global_load_dwordx4 v[58:61], v[16:17], off nt
	s_add_i32 s12, s3, 64
	global_load_dwordx4 v[10:13], v[10:11], off
	v_or_b32_e32 v14, s12, v1
	v_ashrrev_i32_e32 v15, 31, v14
	v_lshl_add_u64 v[14:15], v[14:15], 4, s[6:7]
	s_add_i32 s12, s3, 0x80
	global_load_dwordx4 v[54:57], v[14:15], off nt
	v_or_b32_e32 v14, s12, v1
	v_ashrrev_i32_e32 v15, 31, v14
	v_lshl_add_u64 v[14:15], v[14:15], 4, s[6:7]
	s_add_i32 s12, s3, 0xc0
	global_load_dwordx4 v[98:101], v[14:15], off nt
	v_or_b32_e32 v14, s12, v1
	v_ashrrev_i32_e32 v15, 31, v14
	v_lshl_add_u64 v[14:15], v[14:15], 4, s[6:7]
	s_add_i32 s12, s11, 64
	global_load_dwordx4 v[82:85], v[14:15], off nt
	v_or_b32_e32 v14, s12, v1
	v_ashrrev_i32_e32 v15, 31, v14
	v_lshl_add_u64 v[14:15], v[14:15], 4, s[4:5]
	s_add_i32 s12, s11, 0x80
	global_load_dwordx4 v[34:37], v[14:15], off
	v_or_b32_e32 v14, s12, v1
	s_add_i32 s12, s11, 0xc0
	v_or_b32_e32 v16, s12, v1
	s_add_i32 s12, s11, 0x100
	v_or_b32_e32 v18, s12, v1
	s_add_i32 s12, s11, 0x140
	v_ashrrev_i32_e32 v15, 31, v14
	v_ashrrev_i32_e32 v17, 31, v16
	v_or_b32_e32 v20, s12, v1
	v_lshl_add_u64 v[14:15], v[14:15], 4, s[4:5]
	v_lshl_add_u64 v[16:17], v[16:17], 4, s[4:5]
	v_ashrrev_i32_e32 v21, 31, v20
	s_add_i32 s12, s11, 0x180
	global_load_dwordx4 v[30:33], v[14:15], off
	global_load_dwordx4 v[26:29], v[16:17], off
	v_lshl_add_u64 v[14:15], v[20:21], 4, s[4:5]
	v_or_b32_e32 v20, s12, v1
	v_ashrrev_i32_e32 v21, 31, v20
	s_add_i32 s12, s11, 0x1c0
	v_lshl_add_u64 v[38:39], v[20:21], 4, s[4:5]
	v_or_b32_e32 v20, s12, v1
	v_ashrrev_i32_e32 v21, 31, v20
	s_addk_i32 s11, 0x200
	v_lshl_add_u64 v[40:41], v[20:21], 4, s[4:5]
	v_or_b32_e32 v20, s11, v1
	v_ashrrev_i32_e32 v21, 31, v20
	s_add_i32 s11, s3, 0x100
	v_lshl_add_u64 v[42:43], v[20:21], 4, s[4:5]
	v_or_b32_e32 v20, s11, v1
	s_add_i32 s11, s3, 0x140
	v_or_b32_e32 v16, s11, v1
	v_ashrrev_i32_e32 v17, 31, v16
	s_add_i32 s11, s3, 0x180
	v_lshl_add_u64 v[46:47], v[16:17], 4, s[6:7]
	v_or_b32_e32 v16, s11, v1
	v_ashrrev_i32_e32 v17, 31, v16
	s_add_i32 s11, s3, 0x1c0
	v_lshl_add_u64 v[48:49], v[16:17], 4, s[6:7]
	v_or_b32_e32 v16, s11, v1
	v_ashrrev_i32_e32 v17, 31, v16
	s_add_i32 s11, s3, 0x200
	v_lshl_add_u64 v[50:51], v[16:17], 4, s[6:7]
	v_or_b32_e32 v16, s11, v1
	v_ashrrev_i32_e32 v17, 31, v16
	s_add_i32 s11, s3, 0x240
	v_lshl_add_u64 v[52:53], v[16:17], 4, s[6:7]
	v_or_b32_e32 v16, s11, v1
	v_ashrrev_i32_e32 v17, 31, v16
	s_add_i32 s11, s3, 0x280
	v_ashrrev_i32_e32 v19, 31, v18
	v_ashrrev_i32_e32 v21, 31, v20
	v_lshl_add_u64 v[66:67], v[16:17], 4, s[6:7]
	v_or_b32_e32 v16, s11, v1
	v_lshl_add_u64 v[18:19], v[18:19], 4, s[4:5]
	v_lshl_add_u64 v[44:45], v[20:21], 4, s[6:7]
	v_ashrrev_i32_e32 v17, 31, v16
	s_add_i32 s11, s3, 0x2c0
	global_load_dwordx4 v[22:25], v[18:19], off
	v_lshl_add_u64 v[86:87], v[16:17], 4, s[6:7]
	v_or_b32_e32 v16, s11, v1
	s_add_i32 s11, s3, 0x300
	global_load_dwordx4 v[18:21], v[14:15], off
	global_load_dwordx4 v[62:65], v[44:45], off nt
	v_lshlrev_b32_e32 v14, 4, v0
	s_waitcnt vmcnt(12)
	ds_write_b128 v14, v[6:9]
	v_or_b32_e32 v6, s11, v1
	v_ashrrev_i32_e32 v7, 31, v6
	s_add_i32 s11, s3, 0x340
	v_lshl_add_u64 v[142:143], v[6:7], 4, s[6:7]
	v_or_b32_e32 v6, s11, v1
	v_ashrrev_i32_e32 v7, 31, v6
	s_add_i32 s11, s3, 0x380
	v_lshl_add_u64 v[146:147], v[6:7], 4, s[6:7]
	v_or_b32_e32 v6, s11, v1
	v_ashrrev_i32_e32 v17, 31, v16
	v_ashrrev_i32_e32 v7, 31, v6
	v_lshl_add_u64 v[88:89], v[16:17], 4, s[6:7]
	s_waitcnt vmcnt(9)
	ds_write_b128 v14, v[10:13] offset:8192
	global_load_dwordx4 v[14:17], v[38:39], off
	global_load_dwordx4 v[10:13], v[40:41], off
	v_lshl_add_u64 v[38:39], v[6:7], 4, s[6:7]
	global_load_dwordx4 v[6:9], v[42:43], off
	global_load_dwordx4 v[94:97], v[46:47], off nt
	global_load_dwordx4 v[78:81], v[48:49], off nt
	global_load_dwordx4 v[74:77], v[50:51], off nt
	global_load_dwordx4 v[70:73], v[52:53], off nt
	s_add_i32 s11, s3, 0x3c0
	v_or_b32_e32 v40, s11, v1
	v_ashrrev_i32_e32 v41, 31, v40
	v_mfma_f32_16x16x32_f16 v[102:105], v[58:61], v[2:5], 0
	v_lshl_add_u64 v[40:41], v[40:41], 4, s[6:7]
	global_load_dwordx4 v[66:69], v[66:67], off nt
	s_nop 0
	global_load_dwordx4 v[90:93], v[86:87], off nt
	s_nop 0
	global_load_dwordx4 v[86:89], v[88:89], off nt
	s_nop 0
	global_load_dwordx4 v[50:53], v[142:143], off nt
	global_load_dwordx4 v[46:49], v[146:147], off nt
	global_load_dwordx4 v[42:45], v[38:39], off nt
	s_nop 0
	global_load_dwordx4 v[38:41], v[40:41], off nt
	s_waitcnt vmcnt(22)
	v_mfma_f32_16x16x32_f16 v[106:109], v[54:57], v[2:5], 0
	s_mov_b32 s11, 0x7f000000
	v_mov_b32_e32 v159, 0
	v_mov_b32_e32 v171, 0
	s_waitcnt vmcnt(21)
	v_mfma_f32_16x16x32_f16 v[110:113], v[98:101], v[2:5], 0
	v_mov_b32_e32 v173, 0
	v_mov_b32_e32 v197, 0
	v_mov_b32_e32 v195, 0
	s_waitcnt vmcnt(20)
	v_mfma_f32_16x16x32_f16 v[114:117], v[82:85], v[2:5], 0
	v_mov_b32_e32 v199, 0
	v_min_i32_e32 v102, v102, v103
	v_min_i32_e32 v103, v104, v105
	v_min_i32_e32 v104, v106, v107
	v_min_i32_e32 v105, v108, v109
	v_min_i32_e32 v154, v110, v111
	v_min3_i32 v102, v102, v103, v104
	v_min_i32_e32 v155, v112, v113
	v_min_i32_e32 v114, v114, v115
	v_min3_i32 v102, v102, v105, v154
	s_waitcnt vmcnt(19)
	v_mfma_f32_16x16x32_f16 v[118:121], v[58:61], v[34:37], 0
	v_min_i32_e32 v115, v116, v117
	v_min3_i32 v102, v102, v155, v114
	v_min3_i32 v158, v102, v115, s11
	v_mfma_f32_16x16x32_f16 v[122:125], v[54:57], v[34:37], 0
	v_mov_b32_e32 v204, 0
	s_add_i32 s12, s3, 0x400
	v_mov_b32_e32 v205, 0
	v_mfma_f32_16x16x32_f16 v[126:129], v[98:101], v[34:37], 0
	v_mov_b32_e32 v220, 0
	v_mfma_f32_16x16x32_f16 v[130:133], v[82:85], v[34:37], 0
	s_waitcnt vmcnt(18)
	v_mfma_f32_16x16x32_f16 v[134:137], v[58:61], v[30:33], 0
	v_mfma_f32_16x16x32_f16 v[138:141], v[54:57], v[30:33], 0
	v_mfma_f32_16x16x32_f16 v[142:145], v[98:101], v[30:33], 0
	v_mfma_f32_16x16x32_f16 v[146:149], v[82:85], v[30:33], 0
	s_nop 0
	v_min_i32_e32 v102, v118, v119
	v_min_i32_e32 v103, v120, v121
	v_min_i32_e32 v104, v122, v123
	v_min_i32_e32 v105, v124, v125
	v_min_i32_e32 v114, v126, v127
	v_min3_i32 v102, v102, v103, v104
	v_min_i32_e32 v115, v128, v129
	v_min_i32_e32 v116, v130, v131
	v_min3_i32 v102, v102, v105, v114
	v_min_i32_e32 v117, v132, v133
	v_min3_i32 v102, v102, v115, v116
	s_waitcnt vmcnt(17)
	v_mfma_f32_16x16x32_f16 v[150:153], v[58:61], v[26:29], 0
	v_min3_i32 v170, v102, v117, s11
	v_mfma_f32_16x16x32_f16 v[106:109], v[54:57], v[26:29], 0
	v_mfma_f32_16x16x32_f16 v[110:113], v[98:101], v[26:29], 0
	v_mfma_f32_16x16x32_f16 v[154:157], v[82:85], v[26:29], 0
	s_nop 0
	v_min_i32_e32 v114, v134, v135
	v_min_i32_e32 v115, v136, v137
	v_min_i32_e32 v116, v138, v139
	v_min_i32_e32 v117, v140, v141
	v_min_i32_e32 v122, v142, v143
	v_min3_i32 v114, v114, v115, v116
	v_min_i32_e32 v123, v144, v145
	v_min_i32_e32 v124, v146, v147
	v_min3_i32 v114, v114, v117, v122
	v_min_i32_e32 v125, v148, v149
	v_min3_i32 v114, v114, v123, v124
	s_waitcnt vmcnt(16)
	v_mfma_f32_16x16x32_f16 v[160:163], v[58:61], v[22:25], 0
	v_min3_i32 v172, v114, v125, s11
	v_mfma_f32_16x16x32_f16 v[164:167], v[54:57], v[22:25], 0
	v_mfma_f32_16x16x32_f16 v[118:121], v[98:101], v[22:25], 0
	v_mfma_f32_16x16x32_f16 v[128:131], v[82:85], v[22:25], 0
	s_nop 0
	v_min_i32_e32 v110, v110, v111
	s_waitcnt vmcnt(15)
	v_mfma_f32_16x16x32_f16 v[174:177], v[58:61], v[18:21], 0
	v_min_i32_e32 v111, v112, v113
	v_min_i32_e32 v112, v154, v155
	v_min_i32_e32 v113, v156, v157
	s_waitcnt vmcnt(13)
	v_mfma_f32_16x16x32_f16 v[102:105], v[58:61], v[14:17], 0
	s_waitcnt vmcnt(12)
	v_mfma_f32_16x16x32_f16 v[134:137], v[58:61], v[10:13], 0
	s_waitcnt vmcnt(11)
	v_mfma_f32_16x16x32_f16 v[114:117], v[58:61], v[6:9], 0
	v_min_i32_e32 v58, v150, v151
	v_min_i32_e32 v59, v152, v153
	v_min_i32_e32 v60, v106, v107
	v_min_i32_e32 v61, v108, v109
	v_min3_i32 v58, v58, v59, v60
	v_min3_i32 v58, v58, v61, v110
	v_min3_i32 v58, v58, v111, v112
	v_mfma_f32_16x16x32_f16 v[178:181], v[54:57], v[18:21], 0
	v_min3_i32 v196, v58, v113, s11
	v_mfma_f32_16x16x32_f16 v[182:185], v[98:101], v[18:21], 0
	v_mfma_f32_16x16x32_f16 v[186:189], v[82:85], v[18:21], 0
	s_nop 0
	v_min_i32_e32 v110, v160, v161
	v_min_i32_e32 v111, v162, v163
	v_min_i32_e32 v112, v164, v165
	v_mfma_f32_16x16x32_f16 v[142:145], v[54:57], v[14:17], 0
	v_min_i32_e32 v113, v166, v167
	v_min_i32_e32 v118, v118, v119
	v_min_i32_e32 v119, v120, v121
	v_mfma_f32_16x16x32_f16 v[146:149], v[98:101], v[14:17], 0
	v_min_i32_e32 v120, v128, v129
	v_mfma_f32_16x16x32_f16 v[58:61], v[54:57], v[10:13], 0
	v_mfma_f32_16x16x32_f16 v[122:125], v[54:57], v[6:9], 0
	v_mfma_f32_16x16x32_f16 v[54:57], v[98:101], v[10:13], 0
	v_mfma_f32_16x16x32_f16 v[126:129], v[98:101], v[6:9], 0
	v_min3_i32 v99, v110, v111, v112
	v_min3_i32 v99, v99, v113, v118
	v_min_i32_e32 v98, v130, v131
	v_min3_i32 v99, v99, v119, v120
	v_mfma_f32_16x16x32_f16 v[106:109], v[82:85], v[14:17], 0
	v_min3_i32 v194, v99, v98, s11
	v_mfma_f32_16x16x32_f16 v[138:141], v[82:85], v[10:13], 0
	v_min_i32_e32 v98, v182, v183
	v_min_i32_e32 v99, v184, v185
	v_min_i32_e32 v100, v186, v187
	v_mfma_f32_16x16x32_f16 v[130:133], v[82:85], v[6:9], 0
	v_min_i32_e32 v82, v174, v175
	v_min_i32_e32 v83, v176, v177
	v_min_i32_e32 v84, v178, v179
	v_min_i32_e32 v85, v180, v181
	v_min3_i32 v82, v82, v83, v84
	v_min3_i32 v82, v82, v85, v98
	v_min_i32_e32 v101, v188, v189
	v_min3_i32 v82, v82, v99, v100
	v_min3_i32 v198, v82, v101, s11
	v_mfma_f32_16x16x32_f16 v[150:153], v[62:65], v[2:5], 0
	v_min_i32_e32 v82, v102, v103
	v_min_i32_e32 v83, v104, v105
	v_min_i32_e32 v84, v142, v143
	v_min_i32_e32 v85, v144, v145
	v_min_i32_e32 v98, v146, v147
	v_min3_i32 v82, v82, v83, v84
	v_min_i32_e32 v99, v148, v149
	v_min_i32_e32 v100, v106, v107
	v_min3_i32 v82, v82, v85, v98
	v_min_i32_e32 v101, v108, v109
	v_min3_i32 v82, v82, v99, v100
	v_min3_i32 v203, v82, v101, s11
	v_mfma_f32_16x16x32_f16 v[162:165], v[62:65], v[34:37], 0
	v_min_i32_e32 v58, v58, v59
	v_min_i32_e32 v59, v60, v61
	v_min_i32_e32 v54, v54, v55
	v_mfma_f32_16x16x32_f16 v[166:169], v[62:65], v[30:33], 0
	v_min_i32_e32 v55, v56, v57
	v_min_i32_e32 v56, v138, v139
	v_min_i32_e32 v57, v140, v141
	v_mfma_f32_16x16x32_f16 v[154:157], v[62:65], v[26:29], 0
	v_mfma_f32_16x16x32_f16 v[110:113], v[62:65], v[22:25], 0
	v_mfma_f32_16x16x32_f16 v[118:121], v[62:65], v[18:21], 0
	v_mfma_f32_16x16x32_f16 v[102:105], v[62:65], v[14:17], 0
	v_mfma_f32_16x16x32_f16 v[106:109], v[62:65], v[10:13], 0
	v_mfma_f32_16x16x32_f16 v[98:101], v[62:65], v[6:9], 0
	v_min_i32_e32 v62, v134, v135
	v_min_i32_e32 v63, v136, v137
	v_min3_i32 v58, v62, v63, v58
	v_min3_i32 v54, v58, v59, v54
	v_min3_i32 v54, v54, v55, v56
	v_min3_i32 v202, v54, v57, s11
	v_mov_b32_e32 v54, 0
	s_waitcnt vmcnt(10)
	v_mfma_f32_16x16x32_f16 v[174:177], v[94:97], v[2:5], 0
	v_add_u32_e32 v60, v1, v54
	v_add_u32_e32 v54, s12, v60
	s_add_i32 s12, s3, 0x440
	v_add_u32_e32 v56, s12, v60
	s_add_i32 s12, s3, 0x480
	v_add_u32_e32 v58, s12, v60
	s_add_i32 s12, s3, 0x4c0
	v_ashrrev_i32_e32 v55, 31, v54
	v_ashrrev_i32_e32 v57, 31, v56
	v_ashrrev_i32_e32 v59, 31, v58
	v_add_u32_e32 v60, s12, v60
	s_waitcnt vmcnt(9)
	v_mfma_f32_16x16x32_f16 v[134:137], v[78:81], v[2:5], 0
	v_lshl_add_u64 v[54:55], v[54:55], 4, s[6:7]
	v_lshl_add_u64 v[56:57], v[56:57], 4, s[6:7]
	v_lshl_add_u64 v[58:59], v[58:59], 4, s[6:7]
	s_waitcnt vmcnt(8)
	v_mfma_f32_16x16x32_f16 v[178:181], v[74:77], v[2:5], 0
	v_ashrrev_i32_e32 v61, 31, v60
	v_lshl_add_u64 v[138:139], v[60:61], 4, s[6:7]
	global_load_dwordx4 v[82:85], v[54:55], off nt
	global_load_dwordx4 v[62:65], v[56:57], off nt
	s_nop 0
	global_load_dwordx4 v[58:61], v[58:59], off nt
	s_nop 0
	global_load_dwordx4 v[54:57], v[138:139], off nt
	v_mfma_f32_16x16x32_f16 v[182:185], v[94:97], v[34:37], 0
	v_min_i32_e32 v114, v114, v115
	v_min_i32_e32 v115, v116, v117
	v_min_i32_e32 v116, v122, v123
	v_min_i32_e32 v117, v124, v125
	v_min_i32_e32 v122, v126, v127
	v_min3_i32 v114, v114, v115, v116
	v_min_i32_e32 v123, v128, v129
	v_min_i32_e32 v124, v130, v131
	v_min3_i32 v114, v114, v117, v122
	v_min_i32_e32 v125, v132, v133
	v_min3_i32 v114, v114, v123, v124
	v_mfma_f32_16x16x32_f16 v[206:209], v[78:81], v[34:37], 0
	v_min3_i32 v218, v114, v125, s11
	s_add_i32 s11, s3, 0x500
	s_mov_b32 s12, 0x2aaaaaab
	v_mfma_f32_16x16x32_f16 v[212:215], v[74:77], v[34:37], 0
	s_nop 0
	v_min3_i32 v114, v150, v151, v158
	v_min3_i32 v114, v152, v153, v114
	v_min3_i32 v114, v174, v175, v114
	v_min3_i32 v130, v176, v177, v114
	v_min3_i32 v130, v134, v135, v130
	v_min3_i32 v130, v136, v137, v130
	v_min3_i32 v130, v178, v179, v130
	v_min3_i32 v219, v180, v181, v130
	v_cmp_ge_i32_e32 vcc, v219, v158
	v_mfma_f32_16x16x32_f16 v[224:227], v[94:97], v[30:33], 0
	s_nop 0
	v_cndmask_b32_e32 v221, 1, v159, vcc
	v_mfma_f32_16x16x32_f16 v[228:231], v[78:81], v[30:33], 0
	v_mfma_f32_16x16x32_f16 v[232:235], v[74:77], v[30:33], 0
	s_nop 0
	v_min3_i32 v130, v162, v163, v170
	v_min3_i32 v130, v164, v165, v130
	v_min3_i32 v130, v182, v183, v130
	v_min3_i32 v130, v184, v185, v130
	v_min3_i32 v134, v206, v207, v130
	v_mfma_f32_16x16x32_f16 v[236:239], v[94:97], v[26:29], 0
	v_mfma_f32_16x16x32_f16 v[186:189], v[94:97], v[22:25], 0
	v_mfma_f32_16x16x32_f16 v[146:149], v[94:97], v[18:21], 0
	v_mfma_f32_16x16x32_f16 v[138:141], v[94:97], v[14:17], 0
	v_mfma_f32_16x16x32_f16 v[142:145], v[94:97], v[10:13], 0
	v_mfma_f32_16x16x32_f16 v[126:129], v[94:97], v[6:9], 0
	v_mfma_f32_16x16x32_f16 v[94:97], v[78:81], v[26:29], 0
	v_mfma_f32_16x16x32_f16 v[190:193], v[78:81], v[22:25], 0
	v_mfma_f32_16x16x32_f16 v[174:177], v[78:81], v[18:21], 0
	v_mfma_f32_16x16x32_f16 v[158:161], v[78:81], v[14:17], 0
	v_mfma_f32_16x16x32_f16 v[162:165], v[78:81], v[10:13], 0
	v_mfma_f32_16x16x32_f16 v[130:133], v[78:81], v[6:9], 0
	v_min3_i32 v78, v208, v209, v134
	v_min3_i32 v78, v212, v213, v78
	v_min3_i32 v217, v214, v215, v78
	v_cmp_ge_i32_e32 vcc, v217, v170
	v_mfma_f32_16x16x32_f16 v[122:125], v[74:77], v[26:29], 0
	s_nop 0
	v_cndmask_b32_e32 v222, 1, v171, vcc
	v_mfma_f32_16x16x32_f16 v[114:117], v[74:77], v[22:25], 0
	v_min3_i32 v78, v166, v167, v172
	v_min3_i32 v78, v168, v169, v78
	v_min3_i32 v78, v224, v225, v78
	v_min3_i32 v134, v226, v227, v78
	v_min3_i32 v134, v228, v229, v134
	v_min3_i32 v134, v230, v231, v134
	v_min3_i32 v134, v232, v233, v134
	v_min3_i32 v211, v234, v235, v134
	v_cmp_ge_i32_e32 vcc, v211, v172
	v_mfma_f32_16x16x32_f16 v[182:185], v[74:77], v[18:21], 0
	s_nop 0
	v_cndmask_b32_e32 v213, 1, v173, vcc
	v_mfma_f32_16x16x32_f16 v[178:181], v[74:77], v[14:17], 0
	v_mfma_f32_16x16x32_f16 v[78:81], v[74:77], v[10:13], 0
	v_mfma_f32_16x16x32_f16 v[150:153], v[74:77], v[6:9], 0
	v_min3_i32 v74, v154, v155, v196
	v_min3_i32 v74, v156, v157, v74
	v_min3_i32 v74, v236, v237, v74
	v_min3_i32 v74, v238, v239, v74
	v_min3_i32 v74, v94, v95, v74
	v_min3_i32 v74, v96, v97, v74
	v_min3_i32 v74, v122, v123, v74
	v_min3_i32 v212, v124, v125, v74
	v_cmp_ge_i32_e32 vcc, v212, v196
	s_waitcnt vmcnt(11)
	v_mfma_f32_16x16x32_f16 v[166:169], v[70:73], v[2:5], 0
	v_cndmask_b32_e32 v214, 1, v197, vcc
	v_mfma_f32_16x16x32_f16 v[170:173], v[70:73], v[34:37], 0
	v_min3_i32 v74, v110, v111, v194
	v_min3_i32 v74, v112, v113, v74
	v_min3_i32 v74, v186, v187, v74
	v_min3_i32 v74, v188, v189, v74
	v_min3_i32 v74, v190, v191, v74
	v_min3_i32 v74, v192, v193, v74
	v_min3_i32 v74, v114, v115, v74
	v_min3_i32 v215, v116, v117, v74
	v_cmp_ge_i32_e32 vcc, v215, v194
	v_mfma_f32_16x16x32_f16 v[154:157], v[70:73], v[30:33], 0
	s_nop 0
	v_cndmask_b32_e32 v216, 1, v195, vcc
	v_mfma_f32_16x16x32_f16 v[134:137], v[70:73], v[26:29], 0
	v_min3_i32 v74, v118, v119, v198
	v_min3_i32 v74, v120, v121, v74
	v_mfma_f32_16x16x32_f16 v[122:125], v[70:73], v[22:25], 0
	v_mfma_f32_16x16x32_f16 v[94:97], v[70:73], v[18:21], 0
	v_mfma_f32_16x16x32_f16 v[110:113], v[70:73], v[14:17], 0
	v_mfma_f32_16x16x32_f16 v[114:117], v[70:73], v[10:13], 0
	v_mfma_f32_16x16x32_f16 v[118:121], v[70:73], v[6:9], 0
	v_min3_i32 v70, v146, v147, v74
	v_min3_i32 v70, v148, v149, v70
	v_min3_i32 v70, v174, v175, v70
	v_min3_i32 v70, v176, v177, v70
	v_min3_i32 v70, v182, v183, v70
	v_min3_i32 v223, v184, v185, v70
	v_cmp_ge_i32_e32 vcc, v223, v198
	s_waitcnt vmcnt(10)
	v_mfma_f32_16x16x32_f16 v[186:189], v[66:69], v[2:5], 0
	v_cndmask_b32_e32 v244, 1, v199, vcc
	v_mfma_f32_16x16x32_f16 v[190:193], v[66:69], v[34:37], 0
	v_min3_i32 v70, v102, v103, v203
	v_min3_i32 v70, v104, v105, v70
	v_min3_i32 v70, v138, v139, v70
	v_min3_i32 v70, v140, v141, v70
	v_min3_i32 v70, v158, v159, v70
	v_min3_i32 v70, v160, v161, v70
	v_min3_i32 v70, v178, v179, v70
	v_min3_i32 v245, v180, v181, v70
	v_cmp_ge_i32_e32 vcc, v245, v203
	v_mfma_f32_16x16x32_f16 v[224:227], v[66:69], v[30:33], 0
	s_nop 0
	v_cndmask_b32_e32 v246, 1, v204, vcc
	v_mfma_f32_16x16x32_f16 v[198:201], v[66:69], v[26:29], 0
	v_min3_i32 v70, v106, v107, v202
	v_min3_i32 v70, v108, v109, v70
	v_min3_i32 v70, v142, v143, v70
	v_mfma_f32_16x16x32_f16 v[158:161], v[66:69], v[22:25], 0
	v_min3_i32 v70, v144, v145, v70
	v_min3_i32 v70, v162, v163, v70
	v_min3_i32 v70, v164, v165, v70
	v_mfma_f32_16x16x32_f16 v[146:149], v[66:69], v[18:21], 0
	v_min3_i32 v70, v78, v79, v70
	v_min3_i32 v247, v80, v81, v70
	v_cmp_ge_i32_e32 vcc, v247, v202
	v_mfma_f32_16x16x32_f16 v[138:141], v[66:69], v[14:17], 0
	s_nop 0
	v_cndmask_b32_e32 v248, 1, v205, vcc
	v_mfma_f32_16x16x32_f16 v[106:109], v[66:69], v[10:13], 0
	v_mfma_f32_16x16x32_f16 v[102:105], v[66:69], v[6:9], 0
	v_mov_b32_e32 v66, 0
	s_nop 0
	v_add_u32_e32 v72, v1, v66
	v_add_u32_e32 v66, s11, v72
	s_add_i32 s11, s3, 0x540
	v_add_u32_e32 v68, s11, v72
	s_add_i32 s11, s3, 0x580
	v_add_u32_e32 v70, s11, v72
	s_addk_i32 s3, 0x5c0
	v_ashrrev_i32_e32 v67, 31, v66
	v_ashrrev_i32_e32 v69, 31, v68
	v_ashrrev_i32_e32 v71, 31, v70
	v_add_u32_e32 v72, s3, v72
	s_waitcnt vmcnt(9)
	v_mfma_f32_16x16x32_f16 v[178:181], v[90:93], v[2:5], 0
	v_lshl_add_u64 v[66:67], v[66:67], 4, s[6:7]
	v_lshl_add_u64 v[68:69], v[68:69], 4, s[6:7]
	v_lshl_add_u64 v[70:71], v[70:71], 4, s[6:7]
	s_waitcnt vmcnt(8)
	v_mfma_f32_16x16x32_f16 v[194:197], v[86:89], v[2:5], 0
	v_ashrrev_i32_e32 v73, 31, v72
	v_lshl_add_u64 v[142:143], v[72:73], 4, s[6:7]
	global_load_dwordx4 v[78:81], v[66:67], off nt
	global_load_dwordx4 v[74:77], v[68:69], off nt
	s_nop 0
	global_load_dwordx4 v[70:73], v[70:71], off nt
	s_nop 0
	global_load_dwordx4 v[66:69], v[142:143], off nt
	v_mfma_f32_16x16x32_f16 v[228:231], v[90:93], v[34:37], 0
	v_min3_i32 v98, v98, v99, v218
	v_min3_i32 v98, v100, v101, v98
	v_min3_i32 v98, v126, v127, v98
	v_min3_i32 v98, v128, v129, v98
	v_min3_i32 v98, v130, v131, v98
	v_min3_i32 v98, v132, v133, v98
	v_min3_i32 v98, v150, v151, v98
	v_min3_i32 v249, v152, v153, v98
	v_cmp_ge_i32_e32 vcc, v249, v218
	v_mfma_f32_16x16x32_f16 v[232:235], v[86:89], v[34:37], 0
	s_mul_i32 s3, s15, 6
	v_cndmask_b32_e32 v218, 1, v220, vcc
	v_mfma_f32_16x16x32_f16 v[236:239], v[90:93], v[30:33], 0
	v_min3_i32 v98, v166, v167, v219
	s_mul_i32 s11, s2, 0x90
	v_mfma_f32_16x16x32_f16 v[206:209], v[90:93], v[26:29], 0
	v_mfma_f32_16x16x32_f16 v[182:185], v[90:93], v[22:25], 0
	v_mfma_f32_16x16x32_f16 v[174:177], v[90:93], v[18:21], 0
	v_mfma_f32_16x16x32_f16 v[162:165], v[90:93], v[14:17], 0
	v_mfma_f32_16x16x32_f16 v[142:145], v[90:93], v[10:13], 0
	v_mfma_f32_16x16x32_f16 v[126:129], v[90:93], v[6:9], 0
	v_min3_i32 v90, v168, v169, v98
	v_min3_i32 v90, v186, v187, v90
	v_min3_i32 v98, v188, v189, v90
	v_min3_i32 v98, v178, v179, v98
	v_min3_i32 v98, v180, v181, v98
	v_min3_i32 v98, v194, v195, v98
	v_min3_i32 v220, v196, v197, v98
	v_cmp_ge_i32_e32 vcc, v220, v219
	v_mfma_f32_16x16x32_f16 v[240:243], v[86:89], v[30:33], 0
	s_nop 0
	v_cndmask_b32_e32 v219, 2, v221, vcc
	v_mfma_f32_16x16x32_f16 v[90:93], v[86:89], v[26:29], 0
	v_min3_i32 v98, v170, v171, v217
	v_min3_i32 v98, v172, v173, v98
	v_min3_i32 v98, v190, v191, v98
	v_min3_i32 v98, v192, v193, v98
	v_min3_i32 v98, v228, v229, v98
	v_min3_i32 v98, v230, v231, v98
	v_min3_i32 v98, v232, v233, v98
	v_min3_i32 v221, v234, v235, v98
	v_cmp_ge_i32_e32 vcc, v221, v217
	v_mfma_f32_16x16x32_f16 v[202:205], v[86:89], v[22:25], 0
	s_nop 0
	v_cndmask_b32_e32 v217, 2, v222, vcc
	v_mfma_f32_16x16x32_f16 v[194:197], v[86:89], v[18:21], 0
	v_mfma_f32_16x16x32_f16 v[186:189], v[86:89], v[14:17], 0
	v_mfma_f32_16x16x32_f16 v[166:169], v[86:89], v[10:13], 0
	v_mfma_f32_16x16x32_f16 v[150:153], v[86:89], v[6:9], 0
	v_min3_i32 v86, v154, v155, v211
	v_min3_i32 v86, v156, v157, v86
	v_min3_i32 v86, v224, v225, v86
	v_min3_i32 v86, v226, v227, v86
	v_min3_i32 v86, v236, v237, v86
	v_min3_i32 v86, v238, v239, v86
	v_min3_i32 v86, v240, v241, v86
	v_min3_i32 v222, v242, v243, v86
	v_cmp_ge_i32_e32 vcc, v222, v211
	s_waitcnt vmcnt(11)
	v_mfma_f32_16x16x32_f16 v[170:173], v[50:53], v[2:5], 0
	v_cndmask_b32_e32 v211, 2, v213, vcc
	v_mfma_f32_16x16x32_f16 v[154:157], v[50:53], v[34:37], 0
	v_min3_i32 v86, v134, v135, v212
	v_min3_i32 v86, v136, v137, v86
	v_min3_i32 v86, v198, v199, v86
	v_min3_i32 v86, v200, v201, v86
	v_min3_i32 v86, v206, v207, v86
	v_min3_i32 v86, v208, v209, v86
	v_min3_i32 v86, v90, v91, v86
	v_min3_i32 v198, v92, v93, v86
	v_cmp_ge_i32_e32 vcc, v198, v212
	s_waitcnt vmcnt(10)
	v_mfma_f32_16x16x32_f16 v[134:137], v[46:49], v[2:5], 0
	v_cndmask_b32_e32 v199, 2, v214, vcc
	v_mfma_f32_16x16x32_f16 v[178:181], v[50:53], v[30:33], 0
	v_min3_i32 v122, v122, v123, v215
	v_min3_i32 v122, v124, v125, v122
	v_min3_i32 v122, v158, v159, v122
	v_min3_i32 v122, v160, v161, v122
	v_min3_i32 v122, v182, v183, v122
	v_min3_i32 v122, v184, v185, v122
	v_min3_i32 v122, v202, v203, v122
	v_min3_i32 v200, v204, v205, v122
	v_cmp_ge_i32_e32 vcc, v200, v215
	s_waitcnt vmcnt(9)
	v_mfma_f32_16x16x32_f16 v[158:161], v[42:45], v[2:5], 0
	v_cndmask_b32_e32 v201, 2, v216, vcc
	s_waitcnt vmcnt(8)
	v_mfma_f32_16x16x32_f16 v[182:185], v[38:41], v[2:5], 0
	v_min3_i32 v94, v94, v95, v223
	v_min3_i32 v94, v96, v97, v94
	v_min3_i32 v94, v146, v147, v94
	v_min3_i32 v94, v148, v149, v94
	v_min3_i32 v94, v174, v175, v94
	v_min3_i32 v94, v176, v177, v94
	v_min3_i32 v94, v194, v195, v94
	v_min3_i32 v202, v196, v197, v94
	v_cmp_ge_i32_e32 vcc, v202, v223
	v_mfma_f32_16x16x32_f16 v[146:149], v[46:49], v[34:37], 0
	s_nop 0
	v_cndmask_b32_e32 v203, 2, v244, vcc
	v_mfma_f32_16x16x32_f16 v[174:177], v[42:45], v[34:37], 0
	v_min3_i32 v94, v110, v111, v245
	v_min3_i32 v94, v112, v113, v94
	v_min3_i32 v94, v138, v139, v94
	v_min3_i32 v94, v140, v141, v94
	v_min3_i32 v94, v162, v163, v94
	v_min3_i32 v94, v164, v165, v94
	v_min3_i32 v94, v186, v187, v94
	v_min3_i32 v204, v188, v189, v94
	v_cmp_ge_i32_e32 vcc, v204, v245
	v_mfma_f32_16x16x32_f16 v[194:197], v[38:41], v[34:37], 0
	s_nop 0
	v_cndmask_b32_e32 v205, 2, v246, vcc
	v_mfma_f32_16x16x32_f16 v[110:113], v[46:49], v[30:33], 0
	v_min3_i32 v94, v114, v115, v247
	v_min3_i32 v94, v116, v117, v94
	v_min3_i32 v94, v106, v107, v94
	v_min3_i32 v94, v108, v109, v94
	v_min3_i32 v94, v142, v143, v94
	v_min3_i32 v94, v144, v145, v94
	v_min3_i32 v94, v166, v167, v94
	v_min3_i32 v206, v168, v169, v94
	v_cmp_ge_i32_e32 vcc, v206, v247
	v_mfma_f32_16x16x32_f16 v[190:193], v[50:53], v[26:29], 0
	s_nop 0
	v_cndmask_b32_e32 v207, 2, v248, vcc
	v_mfma_f32_16x16x32_f16 v[138:141], v[46:49], v[26:29], 0
	v_min3_i32 v114, v118, v119, v249
	v_min3_i32 v114, v120, v121, v114
	v_min3_i32 v102, v102, v103, v114
	v_min3_i32 v102, v104, v105, v102
	v_min3_i32 v102, v126, v127, v102
	v_min3_i32 v102, v128, v129, v102
	v_min3_i32 v102, v150, v151, v102
	v_min3_i32 v208, v152, v153, v102
	v_cmp_ge_i32_e32 vcc, v208, v249
	v_mfma_f32_16x16x32_f16 v[118:121], v[42:45], v[30:33], 0
	s_nop 0
	v_cndmask_b32_e32 v209, 2, v218, vcc
	v_mfma_f32_16x16x32_f16 v[126:129], v[38:41], v[30:33], 0
	v_min3_i32 v102, v170, v171, v220
	v_min3_i32 v102, v172, v173, v102
	v_min3_i32 v102, v134, v135, v102
	v_min3_i32 v102, v136, v137, v102
	v_min3_i32 v102, v158, v159, v102
	v_min3_i32 v102, v160, v161, v102
	v_min3_i32 v102, v182, v183, v102
	v_min3_i32 v182, v184, v185, v102
	v_cmp_ge_i32_e32 vcc, v182, v220
	v_mfma_f32_16x16x32_f16 v[142:145], v[42:45], v[26:29], 0
	s_nop 0
	v_cndmask_b32_e32 v183, 3, v219, vcc
	v_mfma_f32_16x16x32_f16 v[150:153], v[38:41], v[26:29], 0
	v_min3_i32 v102, v154, v155, v221
	v_min3_i32 v102, v156, v157, v102
	v_min3_i32 v102, v146, v147, v102
	v_min3_i32 v134, v148, v149, v102
	v_min3_i32 v134, v174, v175, v134
	v_min3_i32 v134, v176, v177, v134
	v_min3_i32 v134, v194, v195, v134
	v_min3_i32 v174, v196, v197, v134
	v_cmp_ge_i32_e32 vcc, v174, v221
	v_mfma_f32_16x16x32_f16 v[130:133], v[50:53], v[22:25], 0
	s_nop 0
	v_cndmask_b32_e32 v175, 3, v217, vcc
	v_mfma_f32_16x16x32_f16 v[186:189], v[46:49], v[22:25], 0
	v_min3_i32 v134, v178, v179, v222
	v_min3_i32 v134, v180, v181, v134
	v_min3_i32 v110, v110, v111, v134
	v_min3_i32 v110, v112, v113, v110
	v_min3_i32 v110, v118, v119, v110
	v_min3_i32 v110, v120, v121, v110
	v_min3_i32 v110, v126, v127, v110
	v_min3_i32 v176, v128, v129, v110
	v_cmp_ge_i32_e32 vcc, v176, v222
	v_mfma_f32_16x16x32_f16 v[166:169], v[42:45], v[22:25], 0
	s_nop 0
	v_cndmask_b32_e32 v177, 3, v211, vcc
	v_mfma_f32_16x16x32_f16 v[170:173], v[38:41], v[22:25], 0
	s_nop 0
	v_min3_i32 v118, v190, v191, v198
	v_mfma_f32_16x16x32_f16 v[162:165], v[38:41], v[18:21], 0
	v_mfma_f32_16x16x32_f16 v[146:149], v[38:41], v[14:17], 0
	v_mfma_f32_16x16x32_f16 v[126:129], v[38:41], v[10:13], 0
	v_mfma_f32_16x16x32_f16 v[110:113], v[38:41], v[6:9], 0
	v_min3_i32 v38, v192, v193, v118
	v_min3_i32 v38, v138, v139, v38
	v_min3_i32 v38, v140, v141, v38
	v_min3_i32 v38, v142, v143, v38
	v_min3_i32 v38, v144, v145, v38
	v_min3_i32 v38, v150, v151, v38
	v_min3_i32 v178, v152, v153, v38
	v_cmp_ge_i32_e32 vcc, v178, v198
	v_mfma_f32_16x16x32_f16 v[98:101], v[50:53], v[18:21], 0
	s_nop 0
	v_cndmask_b32_e32 v179, 3, v199, vcc
	v_mfma_f32_16x16x32_f16 v[122:125], v[46:49], v[18:21], 0
	v_mfma_f32_16x16x32_f16 v[158:161], v[42:45], v[18:21], 0
	s_nop 0
	v_min3_i32 v38, v130, v131, v200
	v_min3_i32 v38, v132, v133, v38
	v_min3_i32 v38, v186, v187, v38
	v_min3_i32 v38, v188, v189, v38
	v_min3_i32 v38, v166, v167, v38
	v_min3_i32 v38, v168, v169, v38
	v_min3_i32 v38, v170, v171, v38
	v_min3_i32 v166, v172, v173, v38
	v_cmp_ge_i32_e32 vcc, v166, v200
	v_mfma_f32_16x16x32_f16 v[86:89], v[50:53], v[14:17], 0
	s_nop 0
	v_cndmask_b32_e32 v167, 3, v201, vcc
	v_mfma_f32_16x16x32_f16 v[106:109], v[46:49], v[14:17], 0
	v_mfma_f32_16x16x32_f16 v[114:117], v[42:45], v[14:17], 0
	s_nop 0
	v_min3_i32 v38, v98, v99, v202
	v_min3_i32 v38, v100, v101, v38
	v_min3_i32 v38, v122, v123, v38
	v_min3_i32 v38, v124, v125, v38
	v_min3_i32 v38, v158, v159, v38
	v_min3_i32 v38, v160, v161, v38
	v_min3_i32 v122, v162, v163, v38
	v_min3_i32 v158, v164, v165, v122
	v_cmp_ge_i32_e32 vcc, v158, v202
	v_mfma_f32_16x16x32_f16 v[90:93], v[50:53], v[10:13], 0
	s_nop 0
	v_cndmask_b32_e32 v159, 3, v203, vcc
	v_mfma_f32_16x16x32_f16 v[94:97], v[46:49], v[10:13], 0
	v_mfma_f32_16x16x32_f16 v[102:105], v[42:45], v[10:13], 0
	s_nop 0
	v_min3_i32 v86, v86, v87, v204
	v_min3_i32 v122, v88, v89, v86
	v_min3_i32 v106, v106, v107, v122
	v_min3_i32 v106, v108, v109, v106
	v_min3_i32 v114, v114, v115, v106
	v_min3_i32 v114, v116, v117, v114
	v_min3_i32 v114, v146, v147, v114
	v_min3_i32 v146, v148, v149, v114
	v_cmp_ge_i32_e32 vcc, v146, v204
	v_mfma_f32_16x16x32_f16 v[50:53], v[50:53], v[6:9], 0
	s_nop 0
	v_cndmask_b32_e32 v147, 3, v205, vcc
	v_mfma_f32_16x16x32_f16 v[46:49], v[46:49], v[6:9], 0
	v_mfma_f32_16x16x32_f16 v[42:45], v[42:45], v[6:9], 0
	s_nop 0
	v_min3_i32 v90, v90, v91, v206
	v_min3_i32 v90, v92, v93, v90
	v_min3_i32 v90, v94, v95, v90
	v_min3_i32 v94, v96, v97, v90
	v_min3_i32 v94, v102, v103, v94
	v_min3_i32 v94, v104, v105, v94
	v_min3_i32 v102, v126, v127, v94
	v_min3_i32 v148, v128, v129, v102
	v_cmp_ge_i32_e32 vcc, v148, v206
	s_waitcnt vmcnt(7)
	v_mfma_f32_16x16x32_f16 v[134:137], v[82:85], v[2:5], 0
	v_cndmask_b32_e32 v149, 3, v207, vcc
	v_mfma_f32_16x16x32_f16 v[138:141], v[82:85], v[34:37], 0
	v_mfma_f32_16x16x32_f16 v[142:145], v[82:85], v[30:33], 0
	v_mfma_f32_16x16x32_f16 v[150:153], v[82:85], v[26:29], 0
	v_mfma_f32_16x16x32_f16 v[154:157], v[82:85], v[22:25], 0
	v_mfma_f32_16x16x32_f16 v[130:133], v[82:85], v[18:21], 0
	v_mfma_f32_16x16x32_f16 v[118:121], v[82:85], v[14:17], 0
	v_mfma_f32_16x16x32_f16 v[98:101], v[82:85], v[10:13], 0
	v_mfma_f32_16x16x32_f16 v[38:41], v[82:85], v[6:9], 0
	s_waitcnt vmcnt(6)
	v_mfma_f32_16x16x32_f16 v[82:85], v[62:65], v[2:5], 0
	s_waitcnt vmcnt(5)
	v_mfma_f32_16x16x32_f16 v[86:89], v[58:61], v[2:5], 0
	s_waitcnt vmcnt(4)
	v_mfma_f32_16x16x32_f16 v[106:109], v[54:57], v[2:5], 0
	s_nop 0
	v_min3_i32 v50, v50, v51, v208
	v_min3_i32 v126, v52, v53, v50
	v_min3_i32 v46, v46, v47, v126
	v_min3_i32 v46, v48, v49, v46
	v_min3_i32 v42, v42, v43, v46
	v_min3_i32 v42, v44, v45, v42
	v_min3_i32 v42, v110, v111, v42
	v_min3_i32 v160, v112, v113, v42
	v_cmp_ge_i32_e32 vcc, v160, v208
	v_mfma_f32_16x16x32_f16 v[114:117], v[62:65], v[34:37], 0
	s_nop 0
	v_cndmask_b32_e32 v161, 3, v209, vcc
	v_mfma_f32_16x16x32_f16 v[122:125], v[58:61], v[34:37], 0
	v_mfma_f32_16x16x32_f16 v[90:93], v[54:57], v[34:37], 0
	s_nop 0
	v_min3_i32 v42, v134, v135, v182
	v_min3_i32 v42, v136, v137, v42
	v_min3_i32 v42, v82, v83, v42
	v_min3_i32 v42, v84, v85, v42
	v_min3_i32 v42, v86, v87, v42
	v_min3_i32 v42, v88, v89, v42
	v_min3_i32 v42, v106, v107, v42
	v_min3_i32 v134, v108, v109, v42
	v_cmp_ge_i32_e32 vcc, v134, v182
	v_mfma_f32_16x16x32_f16 v[94:97], v[62:65], v[30:33], 0
	s_nop 0
	v_cndmask_b32_e32 v135, 4, v183, vcc
	v_mfma_f32_16x16x32_f16 v[102:105], v[58:61], v[30:33], 0
	v_mfma_f32_16x16x32_f16 v[50:53], v[54:57], v[30:33], 0
	v_mfma_f32_16x16x32_f16 v[46:49], v[62:65], v[26:29], 0
	v_mfma_f32_16x16x32_f16 v[110:113], v[62:65], v[22:25], 0
	v_mfma_f32_16x16x32_f16 v[126:129], v[62:65], v[18:21], 0
	v_mfma_f32_16x16x32_f16 v[82:85], v[62:65], v[14:17], 0
	v_mfma_f32_16x16x32_f16 v[86:89], v[62:65], v[10:13], 0
	v_mfma_f32_16x16x32_f16 v[42:45], v[62:65], v[6:9], 0
	v_min3_i32 v62, v138, v139, v174
	v_min3_i32 v106, v140, v141, v62
	v_min3_i32 v106, v114, v115, v106
	v_min3_i32 v106, v116, v117, v106
	v_min3_i32 v114, v122, v123, v106
	v_min3_i32 v114, v124, v125, v114
	v_min3_i32 v90, v90, v91, v114
	v_min3_i32 v122, v92, v93, v90
	v_cmp_ge_i32_e32 vcc, v122, v174
	v_mfma_f32_16x16x32_f16 v[62:65], v[58:61], v[26:29], 0
	s_nop 0
	v_cndmask_b32_e32 v123, 4, v175, vcc
	v_mfma_f32_16x16x32_f16 v[106:109], v[54:57], v[26:29], 0
	s_nop 0
	v_min3_i32 v124, v142, v143, v176
	v_min3_i32 v124, v144, v145, v124
	v_min3_i32 v94, v94, v95, v124
	v_min3_i32 v124, v96, v97, v94
	v_min3_i32 v102, v102, v103, v124
	v_min3_i32 v102, v104, v105, v102
	v_min3_i32 v50, v50, v51, v102
	v_min3_i32 v124, v52, v53, v50
	v_cmp_ge_i32_e32 vcc, v124, v176
	v_mfma_f32_16x16x32_f16 v[90:93], v[58:61], v[22:25], 0
	s_nop 0
	v_cndmask_b32_e32 v125, 4, v177, vcc
	v_mfma_f32_16x16x32_f16 v[114:117], v[54:57], v[22:25], 0
	s_nop 0
	v_min3_i32 v136, v150, v151, v178
	v_min3_i32 v136, v152, v153, v136
	v_min3_i32 v46, v46, v47, v136
	v_min3_i32 v46, v48, v49, v46
	v_min3_i32 v62, v62, v63, v46
	v_min3_i32 v62, v64, v65, v62
	v_min3_i32 v62, v106, v107, v62
	v_min3_i32 v136, v108, v109, v62
	v_cmp_ge_i32_e32 vcc, v136, v178
	v_mfma_f32_16x16x32_f16 v[94:97], v[58:61], v[18:21], 0
	s_nop 0
	v_cndmask_b32_e32 v137, 4, v179, vcc
	v_mfma_f32_16x16x32_f16 v[46:49], v[54:57], v[18:21], 0
	s_nop 0
	v_min3_i32 v138, v154, v155, v166
	v_min3_i32 v138, v156, v157, v138
	v_min3_i32 v110, v110, v111, v138
	v_min3_i32 v110, v112, v113, v110
	v_min3_i32 v90, v90, v91, v110
	v_min3_i32 v90, v92, v93, v90
	v_min3_i32 v110, v114, v115, v90
	v_min3_i32 v138, v116, v117, v110
	v_cmp_ge_i32_e32 vcc, v138, v166
	v_mfma_f32_16x16x32_f16 v[102:105], v[58:61], v[14:17], 0
	v_mov_b32_e32 v154, 0
	v_cndmask_b32_e32 v139, 4, v167, vcc
	v_mfma_f32_16x16x32_f16 v[62:65], v[54:57], v[14:17], 0
	s_nop 0
	v_min3_i32 v114, v130, v131, v158
	v_min3_i32 v130, v132, v133, v114
	v_min3_i32 v126, v126, v127, v130
	v_min3_i32 v126, v128, v129, v126
	v_min3_i32 v94, v94, v95, v126
	v_min3_i32 v94, v96, v97, v94
	v_min3_i32 v46, v46, v47, v94
	v_min3_i32 v126, v48, v49, v46
	v_cmp_ge_i32_e32 vcc, v126, v158
	v_mfma_f32_16x16x32_f16 v[50:53], v[58:61], v[10:13], 0
	s_nop 0
	v_cndmask_b32_e32 v127, 4, v159, vcc
	v_mfma_f32_16x16x32_f16 v[106:109], v[54:57], v[10:13], 0
	s_nop 0
	v_min3_i32 v118, v118, v119, v146
	v_min3_i32 v118, v120, v121, v118
	v_min3_i32 v82, v82, v83, v118
	v_min3_i32 v118, v84, v85, v82
	v_min3_i32 v102, v102, v103, v118
	v_min3_i32 v102, v104, v105, v102
	v_min3_i32 v62, v62, v63, v102
	v_min3_i32 v102, v64, v65, v62
	v_cmp_ge_i32_e32 vcc, v102, v146
	v_mfma_f32_16x16x32_f16 v[58:61], v[58:61], v[6:9], 0
	v_and_b32_e32 v146, 7, v0
	v_cndmask_b32_e32 v103, 4, v147, vcc
	v_mfma_f32_16x16x32_f16 v[54:57], v[54:57], v[6:9], 0
	s_nop 0
	v_min3_i32 v98, v98, v99, v148
	v_min3_i32 v104, v100, v101, v98
	v_min3_i32 v86, v86, v87, v104
	v_min3_i32 v86, v88, v89, v86
	v_min3_i32 v50, v50, v51, v86
	v_min3_i32 v50, v52, v53, v50
	v_min3_i32 v50, v106, v107, v50
	v_min3_i32 v104, v108, v109, v50
	v_cmp_ge_i32_e32 vcc, v104, v148
	s_waitcnt vmcnt(3)
	v_mfma_f32_16x16x32_f16 v[90:93], v[78:81], v[2:5], 0
	v_cndmask_b32_e32 v105, 4, v149, vcc
	s_waitcnt vmcnt(2)
	v_mfma_f32_16x16x32_f16 v[110:113], v[74:77], v[2:5], 0
	s_waitcnt vmcnt(1)
	v_mfma_f32_16x16x32_f16 v[114:117], v[70:73], v[2:5], 0
	s_waitcnt vmcnt(0)
	v_mfma_f32_16x16x32_f16 v[2:5], v[66:69], v[2:5], 0
	s_nop 0
	v_min3_i32 v38, v38, v39, v160
	v_min3_i32 v38, v40, v41, v38
	v_min3_i32 v38, v42, v43, v38
	v_min3_i32 v42, v44, v45, v38
	v_min3_i32 v42, v58, v59, v42
	v_min3_i32 v42, v60, v61, v42
	v_min3_i32 v54, v54, v55, v42
	v_min3_i32 v106, v56, v57, v54
	v_cmp_ge_i32_e32 vcc, v106, v160
	v_mfma_f32_16x16x32_f16 v[46:49], v[78:81], v[34:37], 0
	s_nop 0
	v_cndmask_b32_e32 v107, 4, v161, vcc
	v_mfma_f32_16x16x32_f16 v[94:97], v[74:77], v[34:37], 0
	v_mfma_f32_16x16x32_f16 v[82:85], v[70:73], v[34:37], 0
	v_mfma_f32_16x16x32_f16 v[34:37], v[66:69], v[34:37], 0
	s_nop 0
	v_min3_i32 v54, v90, v91, v134
	v_min3_i32 v58, v92, v93, v54
	v_min3_i32 v58, v110, v111, v58
	v_min3_i32 v58, v112, v113, v58
	v_min3_i32 v90, v114, v115, v58
	v_min3_i32 v90, v116, v117, v90
	v_min3_i32 v2, v2, v3, v90
	v_min3_i32 v91, v4, v5, v2
	v_cmp_ge_i32_e32 vcc, v91, v134
	v_mfma_f32_16x16x32_f16 v[62:65], v[78:81], v[30:33], 0
	s_nop 0
	v_cndmask_b32_e32 v90, 5, v135, vcc
	v_add_u32_e32 v251, s3, v90
	v_lshl_or_b32 v90, v251, 2, v253
	ds_min_u64 v252, v[90:91] offset:16384
	v_mfma_f32_16x16x32_f16 v[98:101], v[74:77], v[30:33], 0
	v_mfma_f32_16x16x32_f16 v[86:89], v[70:73], v[30:33], 0
	v_mfma_f32_16x16x32_f16 v[30:33], v[66:69], v[30:33], 0
	s_nop 0
	v_min3_i32 v46, v46, v47, v122
	v_min3_i32 v46, v48, v49, v46
	v_min3_i32 v46, v94, v95, v46
	v_min3_i32 v92, v96, v97, v46
	v_min3_i32 v82, v82, v83, v92
	v_min3_i32 v82, v84, v85, v82
	v_min3_i32 v34, v34, v35, v82
	v_min3_i32 v93, v36, v37, v34
	v_cmp_ge_i32_e32 vcc, v93, v122
	v_mfma_f32_16x16x32_f16 v[50:53], v[78:81], v[26:29], 0
	s_nop 0
	v_cndmask_b32_e32 v92, 5, v123, vcc
	v_add_u32_e32 v251, s3, v92
	v_lshl_or_b32 v92, v251, 2, v253
	ds_min_u64 v252, v[92:93] offset:16512
	v_mfma_f32_16x16x32_f16 v[38:41], v[74:77], v[26:29], 0
	v_mfma_f32_16x16x32_f16 v[42:45], v[70:73], v[26:29], 0
	v_mfma_f32_16x16x32_f16 v[26:29], v[66:69], v[26:29], 0
	s_nop 0
	v_min3_i32 v62, v62, v63, v124
	v_min3_i32 v62, v64, v65, v62
	v_min3_i32 v62, v98, v99, v62
	v_min3_i32 v62, v100, v101, v62
	v_min3_i32 v86, v86, v87, v62
	v_min3_i32 v86, v88, v89, v86
	v_min3_i32 v30, v30, v31, v86
	v_min3_i32 v95, v32, v33, v30
	v_cmp_ge_i32_e32 vcc, v95, v124
	v_mfma_f32_16x16x32_f16 v[54:57], v[78:81], v[22:25], 0
	s_nop 0
	v_cndmask_b32_e32 v94, 5, v125, vcc
	v_add_u32_e32 v251, s3, v94
	v_lshl_or_b32 v94, v251, 2, v253
	ds_min_u64 v252, v[94:95] offset:16640
	v_mfma_f32_16x16x32_f16 v[58:61], v[74:77], v[22:25], 0
	v_mfma_f32_16x16x32_f16 v[2:5], v[70:73], v[22:25], 0
	v_mfma_f32_16x16x32_f16 v[22:25], v[66:69], v[22:25], 0
	s_nop 0
	v_min3_i32 v50, v50, v51, v136
	v_min3_i32 v50, v52, v53, v50
	v_min3_i32 v38, v38, v39, v50
	v_min3_i32 v38, v40, v41, v38
	v_min3_i32 v38, v42, v43, v38
	v_min3_i32 v38, v44, v45, v38
	v_min3_i32 v26, v26, v27, v38
	v_min3_i32 v51, v28, v29, v26
	v_cmp_ge_i32_e32 vcc, v51, v136
	v_mfma_f32_16x16x32_f16 v[46:49], v[78:81], v[18:21], 0
	s_nop 0
	v_cndmask_b32_e32 v50, 5, v137, vcc
	v_add_u32_e32 v251, s3, v50
	v_lshl_or_b32 v50, v251, 2, v253
	ds_min_u64 v252, v[50:51] offset:16768
	v_mfma_f32_16x16x32_f16 v[82:85], v[74:77], v[18:21], 0
	v_mfma_f32_16x16x32_f16 v[34:37], v[70:73], v[18:21], 0
	v_mfma_f32_16x16x32_f16 v[18:21], v[66:69], v[18:21], 0
	s_nop 0
	v_min3_i32 v42, v54, v55, v138
	v_min3_i32 v52, v56, v57, v42
	v_min3_i32 v52, v58, v59, v52
	v_min3_i32 v52, v60, v61, v52
	v_min3_i32 v2, v2, v3, v52
	v_min3_i32 v2, v4, v5, v2
	v_min3_i32 v2, v22, v23, v2
	v_min3_i32 v53, v24, v25, v2
	v_cmp_ge_i32_e32 vcc, v53, v138
	v_mfma_f32_16x16x32_f16 v[62:65], v[78:81], v[14:17], 0
	s_nop 0
	v_cndmask_b32_e32 v52, 5, v139, vcc
	v_add_u32_e32 v251, s3, v52
	v_lshl_or_b32 v52, v251, 2, v253
	ds_min_u64 v252, v[52:53] offset:16896
	v_mfma_f32_16x16x32_f16 v[30:33], v[74:77], v[14:17], 0
	v_mfma_f32_16x16x32_f16 v[86:89], v[70:73], v[14:17], 0
	v_mfma_f32_16x16x32_f16 v[14:17], v[66:69], v[14:17], 0
	s_nop 0
	v_min3_i32 v46, v46, v47, v126
	v_min3_i32 v46, v48, v49, v46
	v_min3_i32 v54, v82, v83, v46
	v_min3_i32 v54, v84, v85, v54
	v_min3_i32 v34, v34, v35, v54
	v_min3_i32 v34, v36, v37, v34
	v_min3_i32 v18, v18, v19, v34
	v_min3_i32 v19, v20, v21, v18
	v_cmp_ge_i32_e32 vcc, v19, v126
	v_mfma_f32_16x16x32_f16 v[38:41], v[78:81], v[10:13], 0
	s_nop 0
	v_cndmask_b32_e32 v18, 5, v127, vcc
	v_add_u32_e32 v251, s3, v18
	v_lshl_or_b32 v18, v251, 2, v253
	ds_min_u64 v252, v[18:19] offset:17024
	v_mfma_f32_16x16x32_f16 v[26:29], v[74:77], v[10:13], 0
	v_mfma_f32_16x16x32_f16 v[42:45], v[70:73], v[10:13], 0
	v_mfma_f32_16x16x32_f16 v[10:13], v[66:69], v[10:13], 0
	s_nop 0
	v_min3_i32 v20, v62, v63, v102
	v_min3_i32 v20, v64, v65, v20
	v_min3_i32 v20, v30, v31, v20
	v_min3_i32 v20, v32, v33, v20
	v_min3_i32 v20, v86, v87, v20
	v_min3_i32 v20, v88, v89, v20
	v_min3_i32 v14, v14, v15, v20
	v_min3_i32 v15, v16, v17, v14
	v_cmp_ge_i32_e32 vcc, v15, v102
	v_mfma_f32_16x16x32_f16 v[2:5], v[78:81], v[6:9], 0
	v_bfe_u32 v17, v0, 4, 2
	v_cndmask_b32_e32 v14, 5, v103, vcc
	v_add_u32_e32 v251, s3, v14
	v_lshl_or_b32 v14, v251, 2, v253
	ds_min_u64 v252, v[14:15] offset:17152
	v_mfma_f32_16x16x32_f16 v[22:25], v[74:77], v[6:9], 0
	v_mfma_f32_16x16x32_f16 v[46:49], v[70:73], v[6:9], 0
	v_mfma_f32_16x16x32_f16 v[6:9], v[66:69], v[6:9], 0
	s_nop 0
	v_min3_i32 v16, v38, v39, v104
	v_min3_i32 v16, v40, v41, v16
	v_min3_i32 v16, v26, v27, v16
	v_min3_i32 v2, v2, v3, v106
	v_min3_i32 v16, v28, v29, v16
	v_min3_i32 v2, v4, v5, v2
	v_min3_i32 v16, v42, v43, v16
	v_min3_i32 v2, v22, v23, v2
	v_lshlrev_b32_e32 v4, 3, v210
	v_min3_i32 v16, v44, v45, v16
	v_min3_i32 v2, v24, v25, v2
	v_min3_i32 v10, v10, v11, v16
	v_min3_i32 v2, v46, v47, v2
	v_min3_i32 v11, v12, v13, v10
	v_min3_i32 v2, v48, v49, v2
	v_cmp_ge_i32_e32 vcc, v11, v104
	v_min3_i32 v2, v6, v7, v2
	v_cndmask_b32_e32 v10, 5, v105, vcc
	v_add_u32_e32 v251, s3, v10
	v_lshl_or_b32 v10, v251, 2, v253
	ds_min_u64 v252, v[10:11] offset:17280
	v_min3_i32 v3, v8, v9, v2
	v_cmp_ge_i32_e32 vcc, v3, v106
	v_cndmask_b32_e32 v2, 5, v107, vcc
	v_add_u32_e32 v2, s3, v2
	v_bfe_u32 v10, v0, 3, 3
	s_lshl_b32 s3, s15, 3
	v_lshl_or_b32 v2, v2, 2, v17
	v_or_b32_e32 v151, s3, v10
	ds_min_u64 v4, v[2:3] offset:17408
	v_lshlrev_b32_e32 v2, 3, v151
	s_waitcnt lgkmcnt(0)
	s_barrier
	ds_read2st64_b32 v[4:5], v2 offset0:64 offset1:66
	s_add_i32 s2, s3, s11
	s_lshr_b32 s2, s2, 4
	s_add_i32 s2, s2, s8
	s_waitcnt lgkmcnt(0)
	v_ashrrev_i32_e32 v3, 2, v4
	v_mul_hi_i32 v6, v3, s12
	v_lshrrev_b32_e32 v7, 31, v6
	v_add_u32_e32 v6, v6, v7
	v_mul_lo_u32 v7, v6, -6
	v_mul_lo_u32 v6, v6, 24
	v_min_i32_e32 v6, 0xa5, v6
	v_add_lshl_u32 v7, v7, v3, 2
	v_bfe_u32 v3, v0, 2, 1
	v_add3_u32 v152, v6, v3, v7
	v_lshlrev_b32_e32 v6, 2, v4
	v_and_b32_e32 v4, 3, v0
	v_and_or_b32 v153, v6, 12, v4
	v_add_u32_e32 v6, s9, v152
	v_lshl_or_b32 v6, v6, 6, v153
	v_bitop3_b32 v7, s3, 15, v10 bitop3:0xc8
	v_lshl_or_b32 v7, v4, 4, v7
	v_lshl_or_b32 v8, s2, 6, v7
	v_ashrrev_i32_e32 v7, 31, v6
	v_lshl_add_u64 v[6:7], v[6:7], 4, s[6:7]
	v_ashrrev_i32_e32 v9, 31, v8
	v_lshl_add_u64 v[8:9], v[8:9], 4, s[4:5]
	global_load_dwordx4 v[126:129], v[6:7], off
	global_load_dwordx4 v[114:117], v[6:7], off offset:256
	global_load_dwordx4 v[130:133], v[6:7], off offset:2048
	global_load_dwordx4 v[118:121], v[6:7], off offset:2304
	global_load_dwordx4 v[134:137], v[8:9], off
	global_load_dwordx4 v[102:105], v[6:7], off offset:512
	global_load_dwordx4 v[78:81], v[6:7], off offset:768
	global_load_dwordx4 v[106:109], v[6:7], off offset:2560
	global_load_dwordx4 v[82:85], v[6:7], off offset:2816
	v_ashrrev_i32_e32 v6, 2, v5
	v_mul_hi_i32 v7, v6, s12
	v_lshrrev_b32_e32 v11, 31, v7
	v_add_u32_e32 v7, v7, v11
	v_mul_lo_u32 v11, v7, -6
	v_mul_lo_u32 v7, v7, 24
	s_add_i32 s2, s3, 64
	v_min_i32_e32 v7, 0xa5, v7
	v_add_lshl_u32 v6, v11, v6, 2
	s_add_i32 s3, s2, s11
	v_add3_u32 v148, v7, v3, v6
	v_lshlrev_b32_e32 v5, 2, v5
	v_and_or_b32 v149, v5, 12, v4
	v_add_u32_e32 v5, s9, v148
	s_lshr_b32 s3, s3, 4
	v_lshl_or_b32 v6, v5, 6, v149
	s_add_i32 s3, s3, s8
	v_bitop3_b32 v5, s2, 15, v10 bitop3:0xc8
	v_lshl_or_b32 v5, v4, 4, v5
	v_lshl_or_b32 v10, s3, 6, v5
	v_ashrrev_i32_e32 v7, 31, v6
	v_ashrrev_i32_e32 v11, 31, v10
	v_lshl_add_u64 v[6:7], v[6:7], 4, s[6:7]
	v_lshl_add_u64 v[10:11], v[10:11], 4, s[4:5]
	global_load_dwordx4 v[110:113], v[10:11], off
	global_load_dwordx4 v[90:93], v[6:7], off
	global_load_dwordx4 v[62:65], v[6:7], off offset:256
	global_load_dwordx4 v[94:97], v[6:7], off offset:2048
	global_load_dwordx4 v[66:69], v[6:7], off offset:2304
	global_load_dwordx4 v[38:41], v[6:7], off offset:512
	global_load_dwordx4 v[18:21], v[6:7], off offset:768
	global_load_dwordx4 v[42:45], v[6:7], off offset:2560
	global_load_dwordx4 v[22:25], v[6:7], off offset:2816
	s_cmpk_lt_u32 s10, 0x80
	s_cselect_b64 s[2:3], -1, 0
	s_cmpk_gt_u32 s10, 0x7f
	s_cbranch_scc1 .LBB1_4
	v_add_u32_e32 v2, 0x4000, v2
	ds_read_b32 v2, v2 offset:1024
	v_or_b32_e32 v147, 0x80, v151
	v_add_u32_e32 v5, s11, v147
	s_waitcnt lgkmcnt(0)
	v_ashrrev_i32_e32 v6, 2, v2
	v_mul_hi_i32 v7, v6, s12
	v_lshrrev_b32_e32 v8, 31, v7
	v_add_u32_e32 v7, v7, v8
	v_mul_lo_u32 v8, v7, -6
	v_mul_lo_u32 v7, v7, 24
	v_min_i32_e32 v7, 0xa5, v7
	v_add_lshl_u32 v6, v8, v6, 2
	v_add3_u32 v150, v7, v3, v6
	v_lshlrev_b32_e32 v2, 2, v2
	v_lshrrev_b32_e32 v3, 4, v5
	v_and_or_b32 v155, v2, 12, v4
	v_add_u32_e32 v2, s9, v150
	v_add_u32_e32 v3, s8, v3
	v_lshl_or_b32 v2, v2, 6, v155
	v_lshl_or_b32 v4, v4, 4, v151
	v_lshl_or_b32 v4, v3, 6, v4
	v_ashrrev_i32_e32 v3, 31, v2
	v_ashrrev_i32_e32 v5, 31, v4
	v_lshl_add_u64 v[2:3], v[2:3], 4, s[6:7]
	v_lshl_add_u64 v[50:51], v[4:5], 4, s[4:5]
	global_load_dwordx4 v[58:61], v[2:3], off
	global_load_dwordx4 v[46:49], v[2:3], off offset:256
	global_load_dwordx4 v[34:37], v[2:3], off offset:2048
	global_load_dwordx4 v[10:13], v[2:3], off offset:2304
	global_load_dwordx4 v[98:101], v[50:51], off
	global_load_dwordx4 v[30:33], v[2:3], off offset:512
	global_load_dwordx4 v[14:17], v[2:3], off offset:768
	global_load_dwordx4 v[6:9], v[2:3], off offset:2560
	s_nop 0
	global_load_dwordx4 v[2:5], v[2:3], off offset:2816
	s_nop 0
	s_nop 0
	v_lshl_or_b32 v150, v150, 4, v155
	s_branch .LBB1_5
.LBB1_4:
.LBB1_5:
	v_mov_b32_e32 v155, 0
	s_waitcnt vmcnt(13)
	v_dot2c_f32_f16_dpp v155, v134, v126 quad_perm:[0,0,0,0] row_mask:0xf bank_mask:0xf
	v_dot2c_f32_f16_dpp v154, v134, v130 quad_perm:[0,0,0,0] row_mask:0xf bank_mask:0xf
	v_dot2c_f32_f16_dpp v155, v135, v127 quad_perm:[0,0,0,0] row_mask:0xf bank_mask:0xf
	v_dot2c_f32_f16_dpp v154, v135, v131 quad_perm:[0,0,0,0] row_mask:0xf bank_mask:0xf
	v_dot2c_f32_f16_dpp v155, v136, v128 quad_perm:[0,0,0,0] row_mask:0xf bank_mask:0xf
	v_dot2c_f32_f16_dpp v154, v136, v132 quad_perm:[0,0,0,0] row_mask:0xf bank_mask:0xf
	v_dot2c_f32_f16_dpp v155, v137, v129 quad_perm:[0,0,0,0] row_mask:0xf bank_mask:0xf
	v_dot2c_f32_f16_dpp v154, v137, v133 quad_perm:[0,0,0,0] row_mask:0xf bank_mask:0xf
	s_waitcnt vmcnt(13)
	v_dot2c_f32_f16_dpp v155, v134, v114 quad_perm:[1,1,1,1] row_mask:0xf bank_mask:0xf
	v_dot2c_f32_f16_dpp v154, v134, v118 quad_perm:[1,1,1,1] row_mask:0xf bank_mask:0xf
	v_dot2c_f32_f16_dpp v155, v135, v115 quad_perm:[1,1,1,1] row_mask:0xf bank_mask:0xf
	v_dot2c_f32_f16_dpp v154, v135, v119 quad_perm:[1,1,1,1] row_mask:0xf bank_mask:0xf
	v_dot2c_f32_f16_dpp v155, v136, v116 quad_perm:[1,1,1,1] row_mask:0xf bank_mask:0xf
	v_dot2c_f32_f16_dpp v154, v136, v120 quad_perm:[1,1,1,1] row_mask:0xf bank_mask:0xf
	v_dot2c_f32_f16_dpp v155, v137, v117 quad_perm:[1,1,1,1] row_mask:0xf bank_mask:0xf
	v_dot2c_f32_f16_dpp v154, v137, v121 quad_perm:[1,1,1,1] row_mask:0xf bank_mask:0xf
	s_waitcnt vmcnt(10)
	v_dot2c_f32_f16_dpp v155, v134, v102 quad_perm:[2,2,2,2] row_mask:0xf bank_mask:0xf
	v_dot2c_f32_f16_dpp v154, v134, v106 quad_perm:[2,2,2,2] row_mask:0xf bank_mask:0xf
	v_dot2c_f32_f16_dpp v155, v135, v103 quad_perm:[2,2,2,2] row_mask:0xf bank_mask:0xf
	v_dot2c_f32_f16_dpp v154, v135, v107 quad_perm:[2,2,2,2] row_mask:0xf bank_mask:0xf
	v_dot2c_f32_f16_dpp v155, v136, v104 quad_perm:[2,2,2,2] row_mask:0xf bank_mask:0xf
	v_dot2c_f32_f16_dpp v154, v136, v108 quad_perm:[2,2,2,2] row_mask:0xf bank_mask:0xf
	v_dot2c_f32_f16_dpp v155, v137, v105 quad_perm:[2,2,2,2] row_mask:0xf bank_mask:0xf
	v_dot2c_f32_f16_dpp v154, v137, v109 quad_perm:[2,2,2,2] row_mask:0xf bank_mask:0xf
	s_waitcnt vmcnt(9)
	v_dot2c_f32_f16_dpp v155, v134, v78 quad_perm:[3,3,3,3] row_mask:0xf bank_mask:0xf
	v_dot2c_f32_f16_dpp v154, v134, v82 quad_perm:[3,3,3,3] row_mask:0xf bank_mask:0xf
	v_dot2c_f32_f16_dpp v155, v135, v79 quad_perm:[3,3,3,3] row_mask:0xf bank_mask:0xf
	v_dot2c_f32_f16_dpp v154, v135, v83 quad_perm:[3,3,3,3] row_mask:0xf bank_mask:0xf
	v_dot2c_f32_f16_dpp v155, v136, v80 quad_perm:[3,3,3,3] row_mask:0xf bank_mask:0xf
	v_dot2c_f32_f16_dpp v154, v136, v84 quad_perm:[3,3,3,3] row_mask:0xf bank_mask:0xf
	v_dot2c_f32_f16_dpp v155, v137, v81 quad_perm:[3,3,3,3] row_mask:0xf bank_mask:0xf
	v_dot2c_f32_f16_dpp v154, v137, v85 quad_perm:[3,3,3,3] row_mask:0xf bank_mask:0xf
	v_or_b32_e32 v78, 8, v146
	s_nop 0
	v_and_or_b32 v79, v155, -16, v146
	v_and_or_b32 v80, v154, -16, v78
	v_min_i32_e32 v79, v79, v80
	s_nop 1
	v_min_i32_dpp v79, v79, v79 quad_perm:[1,0,3,2] row_mask:0xf bank_mask:0xf bound_ctrl:1
	s_nop 1
	v_min_i32_dpp v79, v79, v79 quad_perm:[2,3,0,1] row_mask:0xf bank_mask:0xf bound_ctrl:1
	s_nop 1
	v_min_i32_dpp v80, v79, v79 row_half_mirror row_mask:0xf bank_mask:0xf bound_ctrl:1
	v_and_b32_e32 v79, 7, v80
	v_cmp_eq_u32_e32 vcc, v146, v79
	v_lshlrev_b32_e32 v79, 2, v151
	s_and_saveexec_b64 s[6:7], vcc
	v_lshlrev_b32_e32 v80, 2, v80
	v_lshl_or_b32 v81, v152, 4, v153
	v_and_b32_e32 v80, 32, v80
	v_add_u32_e32 v80, v81, v80
	ds_write_b32 v79, v80 offset:17536
	s_or_b64 exec, exec, s[6:7]
	v_mov_b32_e32 v80, 0
	v_mov_b32_e32 v81, 0
	s_waitcnt vmcnt(5)
	v_dot2c_f32_f16_dpp v81, v110, v90 quad_perm:[0,0,0,0] row_mask:0xf bank_mask:0xf
	v_dot2c_f32_f16_dpp v80, v110, v94 quad_perm:[0,0,0,0] row_mask:0xf bank_mask:0xf
	v_dot2c_f32_f16_dpp v81, v111, v91 quad_perm:[0,0,0,0] row_mask:0xf bank_mask:0xf
	v_dot2c_f32_f16_dpp v80, v111, v95 quad_perm:[0,0,0,0] row_mask:0xf bank_mask:0xf
	v_dot2c_f32_f16_dpp v81, v112, v92 quad_perm:[0,0,0,0] row_mask:0xf bank_mask:0xf
	v_dot2c_f32_f16_dpp v80, v112, v96 quad_perm:[0,0,0,0] row_mask:0xf bank_mask:0xf
	v_dot2c_f32_f16_dpp v81, v113, v93 quad_perm:[0,0,0,0] row_mask:0xf bank_mask:0xf
	v_dot2c_f32_f16_dpp v80, v113, v97 quad_perm:[0,0,0,0] row_mask:0xf bank_mask:0xf
	s_waitcnt vmcnt(4)
	v_dot2c_f32_f16_dpp v81, v110, v62 quad_perm:[1,1,1,1] row_mask:0xf bank_mask:0xf
	v_dot2c_f32_f16_dpp v80, v110, v66 quad_perm:[1,1,1,1] row_mask:0xf bank_mask:0xf
	v_dot2c_f32_f16_dpp v81, v111, v63 quad_perm:[1,1,1,1] row_mask:0xf bank_mask:0xf
	v_dot2c_f32_f16_dpp v80, v111, v67 quad_perm:[1,1,1,1] row_mask:0xf bank_mask:0xf
	v_dot2c_f32_f16_dpp v81, v112, v64 quad_perm:[1,1,1,1] row_mask:0xf bank_mask:0xf
	v_dot2c_f32_f16_dpp v80, v112, v68 quad_perm:[1,1,1,1] row_mask:0xf bank_mask:0xf
	v_dot2c_f32_f16_dpp v81, v113, v65 quad_perm:[1,1,1,1] row_mask:0xf bank_mask:0xf
	v_dot2c_f32_f16_dpp v80, v113, v69 quad_perm:[1,1,1,1] row_mask:0xf bank_mask:0xf
	s_waitcnt vmcnt(1)
	v_dot2c_f32_f16_dpp v81, v110, v38 quad_perm:[2,2,2,2] row_mask:0xf bank_mask:0xf
	v_dot2c_f32_f16_dpp v80, v110, v42 quad_perm:[2,2,2,2] row_mask:0xf bank_mask:0xf
	v_dot2c_f32_f16_dpp v81, v111, v39 quad_perm:[2,2,2,2] row_mask:0xf bank_mask:0xf
	v_dot2c_f32_f16_dpp v80, v111, v43 quad_perm:[2,2,2,2] row_mask:0xf bank_mask:0xf
	v_dot2c_f32_f16_dpp v81, v112, v40 quad_perm:[2,2,2,2] row_mask:0xf bank_mask:0xf
	v_dot2c_f32_f16_dpp v80, v112, v44 quad_perm:[2,2,2,2] row_mask:0xf bank_mask:0xf
	v_dot2c_f32_f16_dpp v81, v113, v41 quad_perm:[2,2,2,2] row_mask:0xf bank_mask:0xf
	v_dot2c_f32_f16_dpp v80, v113, v45 quad_perm:[2,2,2,2] row_mask:0xf bank_mask:0xf
	s_waitcnt vmcnt(0)
	v_dot2c_f32_f16_dpp v81, v110, v18 quad_perm:[3,3,3,3] row_mask:0xf bank_mask:0xf
	v_dot2c_f32_f16_dpp v80, v110, v22 quad_perm:[3,3,3,3] row_mask:0xf bank_mask:0xf
	v_dot2c_f32_f16_dpp v81, v111, v19 quad_perm:[3,3,3,3] row_mask:0xf bank_mask:0xf
	v_dot2c_f32_f16_dpp v80, v111, v23 quad_perm:[3,3,3,3] row_mask:0xf bank_mask:0xf
	v_dot2c_f32_f16_dpp v81, v112, v20 quad_perm:[3,3,3,3] row_mask:0xf bank_mask:0xf
	v_dot2c_f32_f16_dpp v80, v112, v24 quad_perm:[3,3,3,3] row_mask:0xf bank_mask:0xf
	v_dot2c_f32_f16_dpp v81, v113, v21 quad_perm:[3,3,3,3] row_mask:0xf bank_mask:0xf
	v_dot2c_f32_f16_dpp v80, v113, v25 quad_perm:[3,3,3,3] row_mask:0xf bank_mask:0xf
	s_nop 1
	v_and_or_b32 v18, v81, -16, v146
	v_and_or_b32 v19, v80, -16, v78
	v_min_i32_e32 v18, v18, v19
	s_nop 1
	v_min_i32_dpp v18, v18, v18 quad_perm:[1,0,3,2] row_mask:0xf bank_mask:0xf bound_ctrl:1
	s_nop 1
	v_min_i32_dpp v18, v18, v18 quad_perm:[2,3,0,1] row_mask:0xf bank_mask:0xf bound_ctrl:1
	s_nop 1
	v_min_i32_dpp v18, v18, v18 row_half_mirror row_mask:0xf bank_mask:0xf bound_ctrl:1
	v_and_b32_e32 v19, 7, v18
	v_cmp_eq_u32_e32 vcc, v146, v19
	s_and_saveexec_b64 s[6:7], vcc
	v_lshlrev_b32_e32 v18, 2, v18
	v_lshl_or_b32 v19, v148, 4, v149
	v_and_b32_e32 v18, 32, v18
	v_add_u32_e32 v18, v19, v18
	ds_write_b32 v79, v18 offset:17792
	s_or_b64 exec, exec, s[6:7]
	s_andn2_b64 vcc, exec, s[2:3]
	s_cbranch_vccnz .LBB1_13
	v_mov_b32_e32 v18, 0
	v_mov_b32_e32 v19, 0
	v_dot2c_f32_f16_dpp v19, v98, v58 quad_perm:[0,0,0,0] row_mask:0xf bank_mask:0xf
	v_dot2c_f32_f16_dpp v18, v98, v34 quad_perm:[0,0,0,0] row_mask:0xf bank_mask:0xf
	v_dot2c_f32_f16_dpp v19, v99, v59 quad_perm:[0,0,0,0] row_mask:0xf bank_mask:0xf
	v_dot2c_f32_f16_dpp v18, v99, v35 quad_perm:[0,0,0,0] row_mask:0xf bank_mask:0xf
	v_dot2c_f32_f16_dpp v19, v100, v60 quad_perm:[0,0,0,0] row_mask:0xf bank_mask:0xf
	v_dot2c_f32_f16_dpp v18, v100, v36 quad_perm:[0,0,0,0] row_mask:0xf bank_mask:0xf
	v_dot2c_f32_f16_dpp v19, v101, v61 quad_perm:[0,0,0,0] row_mask:0xf bank_mask:0xf
	v_dot2c_f32_f16_dpp v18, v101, v37 quad_perm:[0,0,0,0] row_mask:0xf bank_mask:0xf
	v_dot2c_f32_f16_dpp v19, v98, v46 quad_perm:[1,1,1,1] row_mask:0xf bank_mask:0xf
	v_dot2c_f32_f16_dpp v18, v98, v10 quad_perm:[1,1,1,1] row_mask:0xf bank_mask:0xf
	v_dot2c_f32_f16_dpp v19, v99, v47 quad_perm:[1,1,1,1] row_mask:0xf bank_mask:0xf
	v_dot2c_f32_f16_dpp v18, v99, v11 quad_perm:[1,1,1,1] row_mask:0xf bank_mask:0xf
	v_dot2c_f32_f16_dpp v19, v100, v48 quad_perm:[1,1,1,1] row_mask:0xf bank_mask:0xf
	v_dot2c_f32_f16_dpp v18, v100, v12 quad_perm:[1,1,1,1] row_mask:0xf bank_mask:0xf
	v_dot2c_f32_f16_dpp v19, v101, v49 quad_perm:[1,1,1,1] row_mask:0xf bank_mask:0xf
	v_dot2c_f32_f16_dpp v18, v101, v13 quad_perm:[1,1,1,1] row_mask:0xf bank_mask:0xf
	v_dot2c_f32_f16_dpp v19, v98, v30 quad_perm:[2,2,2,2] row_mask:0xf bank_mask:0xf
	v_dot2c_f32_f16_dpp v18, v98, v6 quad_perm:[2,2,2,2] row_mask:0xf bank_mask:0xf
	v_dot2c_f32_f16_dpp v19, v99, v31 quad_perm:[2,2,2,2] row_mask:0xf bank_mask:0xf
	v_dot2c_f32_f16_dpp v18, v99, v7 quad_perm:[2,2,2,2] row_mask:0xf bank_mask:0xf
	v_dot2c_f32_f16_dpp v19, v100, v32 quad_perm:[2,2,2,2] row_mask:0xf bank_mask:0xf
	v_dot2c_f32_f16_dpp v18, v100, v8 quad_perm:[2,2,2,2] row_mask:0xf bank_mask:0xf
	v_dot2c_f32_f16_dpp v19, v101, v33 quad_perm:[2,2,2,2] row_mask:0xf bank_mask:0xf
	v_dot2c_f32_f16_dpp v18, v101, v9 quad_perm:[2,2,2,2] row_mask:0xf bank_mask:0xf
	v_dot2c_f32_f16_dpp v19, v98, v14 quad_perm:[3,3,3,3] row_mask:0xf bank_mask:0xf
	v_dot2c_f32_f16_dpp v18, v98, v2 quad_perm:[3,3,3,3] row_mask:0xf bank_mask:0xf
	v_dot2c_f32_f16_dpp v19, v99, v15 quad_perm:[3,3,3,3] row_mask:0xf bank_mask:0xf
	v_dot2c_f32_f16_dpp v18, v99, v3 quad_perm:[3,3,3,3] row_mask:0xf bank_mask:0xf
	v_dot2c_f32_f16_dpp v19, v100, v16 quad_perm:[3,3,3,3] row_mask:0xf bank_mask:0xf
	v_dot2c_f32_f16_dpp v18, v100, v4 quad_perm:[3,3,3,3] row_mask:0xf bank_mask:0xf
	v_dot2c_f32_f16_dpp v19, v101, v17 quad_perm:[3,3,3,3] row_mask:0xf bank_mask:0xf
	v_dot2c_f32_f16_dpp v18, v101, v5 quad_perm:[3,3,3,3] row_mask:0xf bank_mask:0xf
	s_nop 1
	v_and_or_b32 v2, v19, -16, v146
	v_and_or_b32 v3, v18, -16, v78
	v_min_i32_e32 v2, v2, v3
	s_nop 1
	v_min_i32_dpp v2, v2, v2 quad_perm:[1,0,3,2] row_mask:0xf bank_mask:0xf bound_ctrl:1
	s_nop 1
	v_min_i32_dpp v2, v2, v2 quad_perm:[2,3,0,1] row_mask:0xf bank_mask:0xf bound_ctrl:1
	s_nop 1
	v_min_i32_dpp v2, v2, v2 row_half_mirror row_mask:0xf bank_mask:0xf bound_ctrl:1
	v_and_b32_e32 v3, 7, v2
	v_cmp_eq_u32_e32 vcc, v146, v3
	s_and_saveexec_b64 s[2:3], vcc
	v_lshlrev_b32_e32 v2, 2, v2
	v_and_b32_e32 v2, 32, v2
	v_lshlrev_b32_e32 v3, 2, v147
	v_add_u32_e32 v2, v2, v150
	ds_write_b32 v3, v2 offset:17536
	s_or_b64 exec, exec, s[2:3]
